# 7 layer-0 tail items per wave in the attention stream on the stacked variant (input-projection staging range ends at 0x8800)
# speedup vs baseline: 1.0231x; 1.0029x over previous
; #define LAS __attribute__((address_space(3)))
; #define WAIT_BAR(N) asm volatile("s_waitcnt vmcnt(" #N ") lgkmcnt(0)\n\ts_barrier" ::: "memory")
; #define DMA_K(t, slot) do { const bf16_t* sb_ = Kh + (long)(t) * KVBLK * DMK; glds16<0>(sb_, kvoff, (unsigned)__builtin_amdgcn_readfirstlane(kdst + (slot))); glds16<0>(sb_ + 64, kvoff, (unsigned)__builtin_amdgcn_readfirstlane(kdst + 8192 + (slot))); } while (0)
; template <int THRL> ...
;     ...
;   const bf16_t* Qw = Q + (size_t)(CTXL + qb * 128 + wq * QBLK) * DMK + head * 128 + comp * 64;
;   const bf16_t* Kh = K + head * 128; const bf16_t* Vh = V + head * 128;
;   const unsigned lds0 = (unsigned)(uintptr_t)shm;
;   LAS float* wsf = (LAS float*)(shm + LDS_WS) + wid * 64;
;   const unsigned kvoff = (unsigned)(lane * DMK + wid * 8) * 2u;
;   const unsigned vvoff = (unsigned)((16 * (wid & 3) + (lane >> 2)) * DMK + (wid >> 2) * 32 + (lane & 3) * 8) * 2u;
;   const unsigned kdst = lds0 + LDS_K + wid * 1024, vdst = lds0 + LDS_V + wid * 1024;
;     ...
;   const int vb0 = (int)(lds0 + LDS_V) + ((lane >> 4) & 1) * 32 + (lane & 3) * 8 + (4 * hi + ((lane & 15) >> 2)) * 64;
;   bf16x8 kf[8];
;   const lds_cptr shm3 = (lds_cptr)shm; const lds_cptr kp0 = shm3 + LDS_K + comp * 8192 + hi * 1024 + r32 * 16;
;   const lds_cptr vp0 = shm3 + LDS_V + ((lane >> 4) & 1) * 32 + (lane & 3) * 8 + (4 * hi + ((lane & 15) >> 2)) * 64;
;   DMA_K(0, 0); DMA_V(0, 0); DMA_K(1, SLOTB);
;   bf16x8 qr[4];
; #pragma unroll
;   for (int d0 = 0; d0 < 4; ++d0) qr[d0] = *reinterpret_cast<const bf16x8*>(&Qw[(long)r32 * DMK + d0 * 16 + hi * 8]);
;   float mhat = 0.f, l_reg = 0.f; f32x16 o[4]; o[0] = f32x16{}; o[1] = f32x16{}; o[2] = f32x16{}; o[3] = f32x16{}; f32x16 negm = f32x16{}; asm volatile("" : "+v"(negm));
;   bool resc = false;
;     ...
;   f32x16 pA0, pA1, pB0, pB1;
;   int sl_prev = 0, sl_cur = 0, sl_next = SLOTB;
;     ...
;   DMA_K(2, 2 * SLOTB);
;   WAIT_BAR(6);
;   qkt(pA0, pA1, kp0, qr, negm); asm volatile("s_nop 15\n\ts_nop 7" : "+v"(pA0), "+v"(pA1));
;   const lds_cptr qp = shm3 + LDS_Q + wid * 4096 + lane * 16;
; #pragma unroll
;   for (int d0 = 0; d0 < 4; ++d0) *(LAS bf16x8*)(shm + LDS_Q + wid * 4096 + lane * 16 + d0 * 1024) = qr[d0];
;   START(pA0, pA1);
; #pragma unroll
;   for (int r = 0; r < 16; ++r) pA1[r] = __builtin_amdgcn_exp2f(pA1[r]);
;   WAIT_BAR(0);
.LBB0_527:
	s_lshl_b32 s0, s28, 1
	s_and_b32 s0, s0, 0x700
	s_add_u32 s33, s26, s0
	s_addc_u32 s53, s27, 0
	s_bfe_u32 s41, s39, 0x20006
	s_lshl_b32 s0, s36, 4
	s_and_b32 s37, s0, 0xffffff80
	s_lshl_b32 s0, s41, 5
	s_or_b32 s0, s37, s0
	s_addk_i32 s0, 0x100
	s_ashr_i32 s1, s0, 31
	s_lshr_b32 s40, s39, 6
	s_lshr_b32 s42, s39, 8
	s_lshl_b64 s[0:1], s[0:1], 11
	s_add_u32 s0, s5, s0
	s_addc_u32 s1, s17, s1
	s_lshl_b32 s2, s36, 7
	s_and_b32 s14, s2, 0x380
	s_lshl_b32 s8, s14, 1
	s_add_u32 s0, s0, s8
	s_addc_u32 s1, s1, 0
	s_lshl_b32 s43, s42, 6
	s_lshl_b32 s2, s42, 7
	s_add_u32 s2, s0, s2
	s_addc_u32 s3, s1, 0
	s_add_u32 s20, s22, s8
	s_addc_u32 s21, s23, 0
	s_add_u32 s8, s24, s8
	s_addc_u32 s9, s25, 0
	s_lshl_b32 s0, s41, 15
	s_add_i32 s0, s0, s43
	v_add_u32_e32 v235, s0, v219
	s_lshl_b32 s0, s40, 10
	s_add_i32 s49, s0, 0
	s_and_b32 s1, s39, 0x3fffffc0
	s_lshl_b32 s38, s40, 4
	s_add_i32 s46, s49, 0xc000
	s_add_u32 s44, s20, 0x80
	v_add_u32_e32 v237, s38, v218
	s_mov_b32 s0, m0
	s_mov_b32 m0, s49
	s_nop 0
	global_load_lds_dwordx4 v237, s[20:21] offset:0
	s_mov_b32 m0, s0
	s_addc_u32 s45, s21, 0
	s_add_i32 s54, s49, 0x2000
	s_mov_b32 s0, m0
	s_mov_b32 m0, s54
	s_nop 0
	global_load_lds_dwordx4 v237, s[44:45] offset:0
	s_mov_b32 m0, s0
	s_add_u32 s50, s8, 0x80
	s_mov_b32 s0, m0
	s_mov_b32 m0, s46
	s_nop 0
	global_load_lds_dwordx4 v235, s[8:9] offset:0
	s_mov_b32 m0, s0
	s_addc_u32 s51, s9, 0
	s_add_i32 s45, s49, 0xe000
	s_mov_b32 s0, m0
	s_mov_b32 m0, s45
	s_nop 0
	global_load_lds_dwordx4 v235, s[50:51] offset:0
	s_mov_b32 m0, s0
	s_add_u32 s50, s20, 0x20000
	s_addc_u32 s51, s21, 0
	s_add_i32 s52, s49, 0x4000
	s_mov_b32 s0, m0
	s_mov_b32 m0, s52
	s_nop 0
	global_load_lds_dwordx4 v237, s[50:51] offset:0
	s_mov_b32 m0, s0
	s_add_u32 s56, s20, 0x20080
	s_addc_u32 s57, s21, 0
	s_add_i32 s51, s49, 0x6000
	s_mov_b32 s0, m0
	s_mov_b32 m0, s51
	s_nop 0
	global_load_lds_dwordx4 v237, s[56:57] offset:0
	s_mov_b32 m0, s0
	global_load_dwordx4 v[66:69], v229, s[2:3]
	global_load_dwordx4 v[70:73], v229, s[2:3] offset:32
	global_load_dwordx4 v[74:77], v229, s[2:3] offset:64
	global_load_dwordx4 v[78:81], v229, s[2:3] offset:96
	v_mov_b64_e32 v[48:49], v[32:33]
	s_add_u32 s2, s20, 0x40000
	v_mov_b64_e32 v[46:47], v[30:31]
	v_mov_b64_e32 v[44:45], v[28:29]
	v_mov_b64_e32 v[42:43], v[26:27]
	v_mov_b64_e32 v[40:41], v[24:25]
	v_mov_b64_e32 v[38:39], v[22:23]
	v_mov_b64_e32 v[36:37], v[20:21]
	v_mov_b64_e32 v[34:35], v[18:19]
	s_addc_u32 s3, s21, 0
	s_add_i32 s48, s49, 0x8000
	s_mov_b32 s0, m0
	s_mov_b32 m0, s48
	s_nop 0
	global_load_lds_dwordx4 v237, s[2:3] offset:0
	s_mov_b32 m0, s0
	s_add_u32 s2, s20, 0x40080
	s_addc_u32 s3, s21, 0
	s_add_i32 s47, s49, 0xa000
	s_mov_b32 s0, m0
	s_mov_b32 m0, s47
	s_nop 0
	global_load_lds_dwordx4 v237, s[2:3] offset:0
	s_mov_b32 m0, s0
	v_lshl_add_u32 v236, s42, 13, v221
	s_waitcnt vmcnt(6) lgkmcnt(0)
	s_barrier
	ds_read_b128 v[4:7], v236
	s_lshl_b32 s2, s40, 12
	v_add_u32_e32 v233, s2, v222
	s_lshl_b32 s1, s1, 2
	s_add_i32 s50, s1, 0
	s_add_i32 s50, s50, 0x18000
	s_add_u32 s2, s20, 0x60000
	s_addc_u32 s3, s21, 0
	v_mov_b32_e32 v3, v2
	v_mov_b32_e32 v12, v2
	v_mov_b32_e32 v13, v2
	s_movk_i32 s57, 0x4000
	s_mov_b32 s0, 0
	s_mov_b32 s55, 0x8000
	v_lshl_add_u32 v232, v217, 2, s50
	v_mov_b32_e32 v238, 0
	s_mov_b32 s56, -1
	s_waitcnt vmcnt(3) lgkmcnt(0)
	v_mfma_f32_32x32x16_bf16 v[50:65], v[4:7], v[66:69], v[34:49]
	ds_read_b128 v[4:7], v236 offset:512
	s_waitcnt lgkmcnt(0)
	v_mfma_f32_32x32x16_bf16 v[34:49], v[4:7], v[66:69], v[34:49]
	ds_read_b128 v[4:7], v236 offset:2048
	s_waitcnt vmcnt(2) lgkmcnt(0)
	v_mfma_f32_32x32x16_bf16 v[50:65], v[4:7], v[70:73], v[50:65]
	ds_read_b128 v[4:7], v236 offset:2560
	s_waitcnt lgkmcnt(0)
	v_mfma_f32_32x32x16_bf16 v[34:49], v[4:7], v[70:73], v[34:49]
	ds_read_b128 v[4:7], v236 offset:4096
	ds_read_b128 v[8:11], v236 offset:4608
	ds_read_b128 v[82:85], v236 offset:6656
	ds_read_b128 v[14:17], v236 offset:6144
	s_waitcnt vmcnt(1) lgkmcnt(3)
	v_mfma_f32_32x32x16_bf16 v[50:65], v[4:7], v[74:77], v[50:65]
	v_mov_b32_e32 v4, v2
	v_mov_b32_e32 v5, v2
	v_mov_b32_e32 v6, v2
	v_mov_b32_e32 v7, v2
	s_waitcnt lgkmcnt(2)
	v_mfma_f32_32x32x16_bf16 v[34:49], v[8:11], v[74:77], v[34:49]
	v_mov_b32_e32 v8, v2
	v_mov_b32_e32 v9, v2
	v_mov_b32_e32 v10, v2
	v_mov_b32_e32 v11, v2
	s_waitcnt vmcnt(0) lgkmcnt(0)
	v_mfma_f32_32x32x16_bf16 v[50:65], v[14:17], v[78:81], v[50:65]
	v_mov_b32_e32 v16, v2
	v_mov_b32_e32 v17, v2
	v_mov_b32_e32 v14, v2
	v_mov_b32_e32 v15, v2
	v_mfma_f32_32x32x16_bf16 v[34:49], v[82:85], v[78:81], v[34:49]
	s_nop 15
	s_nop 7
	ds_write_b128 v233, v[66:69]
	ds_write_b128 v233, v[70:73] offset:1024
	ds_write_b128 v233, v[74:77] offset:2048
	ds_write_b128 v233, v[78:81] offset:3072
	v_max3_f32 v66, v50, v51, v34
	v_max3_f32 v67, v52, v53, v35
	v_mov_b64_e32 v[96:97], v[16:17]
	v_max3_f32 v66, v66, v36, v37
	v_max3_f32 v67, v67, v56, v57
	v_mov_b64_e32 v[94:95], v[14:15]
	v_max3_f32 v66, v66, v54, v55
	v_max3_f32 v67, v67, v40, v41
	v_mov_b64_e32 v[92:93], v[12:13]
	v_max3_f32 v66, v66, v38, v39
	v_max3_f32 v67, v67, v60, v61
	v_mov_b64_e32 v[90:91], v[10:11]
	v_max3_f32 v66, v66, v58, v59
	v_max3_f32 v67, v67, v44, v45
	v_mov_b64_e32 v[88:89], v[8:9]
	v_max3_f32 v66, v66, v42, v43
	v_max3_f32 v67, v67, v64, v65
	v_mov_b64_e32 v[86:87], v[6:7]
	v_max3_f32 v66, v66, v62, v63
	v_max3_f32 v67, v67, v48, v49
	v_mov_b64_e32 v[84:85], v[4:5]
	v_max3_f32 v66, v66, v46, v47
	v_mov_b64_e32 v[82:83], v[2:3]
	v_max_f32_e32 v66, v66, v67
	s_nop 0
	v_mov_b32_e32 v67, v66
	s_nop 1
	v_permlane32_swap_b32_e32 v66, v67
	v_max_f32_e32 v66, v66, v67
	s_nop 0
	v_add_f32_e32 v234, v2, v66
	v_sub_f32_e32 v50, v50, v66
	v_sub_f32_e32 v34, v34, v66
	v_sub_f32_e32 v51, v51, v66
	v_sub_f32_e32 v35, v35, v66
	v_sub_f32_e32 v52, v52, v66
	s_nop 0
	v_xor_b32_e32 v98, 0x80000000, v234
	v_mov_b32_e32 v99, v98
	v_mov_b32_e32 v100, v98
	v_mov_b32_e32 v101, v98
	v_mov_b32_e32 v102, v98
	v_mov_b32_e32 v103, v98
	v_mov_b32_e32 v104, v98
	v_mov_b32_e32 v105, v98
	v_mov_b32_e32 v106, v98
	v_mov_b32_e32 v107, v98
	v_mov_b32_e32 v108, v98
	v_mov_b32_e32 v109, v98
	v_mov_b32_e32 v110, v98
	v_mov_b32_e32 v111, v98
	v_mov_b32_e32 v112, v98
	v_mov_b32_e32 v113, v98
	s_waitcnt vmcnt(0) lgkmcnt(0)
	s_barrier
; #define LAS __attribute__((address_space(3)))
; #define WAIT_BAR(N) asm volatile("s_waitcnt vmcnt(" #N ") lgkmcnt(0)\n\ts_barrier" ::: "memory")
; #define DMA_K(t, slot) do { const bf16_t* sb_ = Kh + (long)(t) * KVBLK * DMK; glds16<0>(sb_, kvoff, (unsigned)__builtin_amdgcn_readfirstlane(kdst + (slot))); glds16<0>(sb_ + 64, kvoff, (unsigned)__builtin_amdgcn_readfirstlane(kdst + 8192 + (slot))); } while (0)
; #define DMA_V(t, slot) do { const bf16_t* sb_ = Vh + (long)(t) * KVBLK * DMK; glds16<0>(sb_, vvoff, (unsigned)__builtin_amdgcn_readfirstlane(vdst + (slot))); glds16<0>(sb_ + 64, vvoff, (unsigned)__builtin_amdgcn_readfirstlane(vdst + 8192 + (slot))); } while (0)
; #define ROT() do { sl_prev = sl_cur; sl_cur = sl_next; sl_next = (sl_next == (NSLOT - 1) * SLOTB) ? 0 : sl_next + SLOTB; } while (0)
;     __device__ __forceinline__ const float* w_gate() const { return (const float*)ld(21); }
;     __device__ __forceinline__ const float* w_up() const { return (const float*)ld(22); }
; template <int THRL> ...
;     ...
;   DMA_K(3, 0); DMA_V(1, SLOTB);
;   ROT();
;   kload8(kf, kp0 + sl_cur);
;   WAIT_BAR(4);
;   s16x4 vlo[4], vhi[4]; u32x4 pw0, pw1, pw2, pw3;
; __device__ __forceinline__ void convert_moe_items(const Ctx& a, int layer, LAS unsigned char* lds, int it0, int it1, int widx, int nw, int wave, int lane) {
;     LAS float* scr = (LAS float*)(lds + wave * 16384);
;     bf16_t* WGU = (bf16_t*)(a.ws() + WS_WGU + (size_t)layer * WGU_BYTES); bf16_t* WD = (bf16_t*)(a.ws() + WS_WD + (size_t)layer * WD_BYTES);
;     constexpr int I_G = (DM / 64) * (FE / 32), I_D = (FE / 64) * (DM / 32);
;     constexpr int PER_E = 2 * I_G + I_D;
;     const float *wg = a.w_gate(), *wu = a.w_up(), *wd = a.w_down();
;     auto decode = [&](int it) { CvtItem d; const int e = it / PER_E; int r = it % PER_E; const size_t eo = ((size_t)layer * NE + e) * (size_t)DM * FE;
;         if (r < I_G)          { d.src = wg + eo; d.dst = WGU; d.N = FE; d.K = DM; d.row_off = e * 2048; d.ilv = 1; }
;         else if (r < 2 * I_G) { r -= I_G; d.src = wu + eo; d.dst = WGU; d.N = FE; d.K = DM; d.row_off = e * 2048 + 128; d.ilv = 1; }
;         else                  { r -= 2 * I_G; d.src = wd + eo; d.dst = WD; d.N = DM; d.K = FE; d.row_off = e * 2048; d.ilv = 0; }
;         const int nblk = d.N / 32; d.k0 = 64 * (r / nblk); d.n0 = 32 * (r % nblk); return d; };
;     int it = it0 + widx;
	s_mov_b32 s1, m0
	s_mov_b32 m0, s49
	s_nop 0
	global_load_lds_dwordx4 v237, s[2:3] offset:0
	s_mov_b32 m0, s1
	s_add_u32 s2, s20, 0x60080
	s_addc_u32 s3, s21, 0
	s_mov_b32 s1, m0
	s_mov_b32 m0, s54
	s_nop 0
	global_load_lds_dwordx4 v237, s[2:3] offset:0
	s_mov_b32 m0, s1
	s_add_u32 s2, s8, 0x20000
	s_addc_u32 s3, s9, 0
	s_add_i32 s44, s49, 0x10000
	s_mov_b32 s1, m0
	s_mov_b32 m0, s44
	s_nop 0
	global_load_lds_dwordx4 v235, s[2:3] offset:0
	s_mov_b32 m0, s1
	s_add_u32 s2, s8, 0x20080
	s_addc_u32 s3, s9, 0
	s_add_i32 s43, s49, 0x12000
	s_mov_b32 s1, m0
	s_mov_b32 m0, s43
	s_nop 0
	global_load_lds_dwordx4 v235, s[2:3] offset:0
	s_mov_b32 m0, s1
	ds_read_b128 v[146:149], v236 offset:16384
	ds_read_b128 v[202:205], v236 offset:16896
	ds_read_b128 v[206:209], v236 offset:18432
	ds_read_b128 v[190:193], v236 offset:18944
	ds_read_b128 v[198:201], v236 offset:20480
	ds_read_b128 v[186:189], v236 offset:20992
	ds_read_b128 v[182:185], v236 offset:22528
	ds_read_b128 v[178:181], v236 offset:23040
	v_sub_f32_e32 v36, v36, v66
	v_sub_f32_e32 v53, v53, v66
	v_sub_f32_e32 v37, v37, v66
	v_sub_f32_e32 v54, v54, v66
	v_sub_f32_e32 v38, v38, v66
	v_sub_f32_e32 v55, v55, v66
	v_sub_f32_e32 v39, v39, v66
	v_sub_f32_e32 v56, v56, v66
	v_sub_f32_e32 v40, v40, v66
	v_sub_f32_e32 v57, v57, v66
	v_sub_f32_e32 v41, v41, v66
	v_sub_f32_e32 v58, v58, v66
	v_sub_f32_e32 v42, v42, v66
	v_sub_f32_e32 v59, v59, v66
	v_sub_f32_e32 v43, v43, v66
	v_sub_f32_e32 v60, v60, v66
	v_sub_f32_e32 v44, v44, v66
	v_sub_f32_e32 v61, v61, v66
	v_sub_f32_e32 v45, v45, v66
	v_sub_f32_e32 v62, v62, v66
	v_sub_f32_e32 v46, v46, v66
	v_sub_f32_e32 v63, v63, v66
	v_sub_f32_e32 v47, v47, v66
	v_sub_f32_e32 v64, v64, v66
	v_sub_f32_e32 v48, v48, v66
	v_sub_f32_e32 v65, v65, v66
	v_sub_f32_e32 v49, v49, v66
	v_exp_f32_e32 v130, v50
	v_exp_f32_e32 v131, v51
	v_exp_f32_e32 v132, v52
	v_exp_f32_e32 v133, v53
	v_exp_f32_e32 v134, v54
	v_exp_f32_e32 v135, v55
	v_exp_f32_e32 v136, v56
	v_exp_f32_e32 v137, v57
	v_exp_f32_e32 v138, v58
	v_exp_f32_e32 v139, v59
	v_exp_f32_e32 v140, v60
	v_exp_f32_e32 v141, v61
	v_exp_f32_e32 v142, v62
	v_exp_f32_e32 v143, v63
	v_exp_f32_e32 v144, v64
	v_exp_f32_e32 v145, v65
	v_exp_f32_e32 v114, v34
	v_exp_f32_e32 v115, v35
	v_exp_f32_e32 v116, v36
	v_exp_f32_e32 v117, v37
	v_exp_f32_e32 v118, v38
	v_exp_f32_e32 v119, v39
	v_exp_f32_e32 v120, v40
	v_exp_f32_e32 v121, v41
	v_exp_f32_e32 v122, v42
	v_exp_f32_e32 v123, v43
	v_exp_f32_e32 v124, v44
	v_exp_f32_e32 v125, v45
	v_exp_f32_e32 v126, v46
	v_exp_f32_e32 v127, v47
	v_exp_f32_e32 v128, v48
	v_exp_f32_e32 v129, v49
	s_waitcnt vmcnt(4) lgkmcnt(0)
	s_barrier
	v_mov_b64_e32 v[80:81], v[16:17]
	v_mov_b64_e32 v[48:49], v[16:17]
	v_mov_b64_e32 v[64:65], v[16:17]
	v_mov_b64_e32 v[78:79], v[14:15]
	v_mov_b64_e32 v[76:77], v[12:13]
	v_mov_b64_e32 v[74:75], v[10:11]
	v_mov_b64_e32 v[72:73], v[8:9]
	v_mov_b64_e32 v[70:71], v[6:7]
	v_mov_b64_e32 v[68:69], v[4:5]
	v_mov_b64_e32 v[66:67], v[2:3]
	v_mov_b64_e32 v[46:47], v[14:15]
	v_mov_b64_e32 v[44:45], v[12:13]
	v_mov_b64_e32 v[42:43], v[10:11]
	v_mov_b64_e32 v[40:41], v[8:9]
	v_mov_b64_e32 v[38:39], v[6:7]
	v_mov_b64_e32 v[36:37], v[4:5]
	v_mov_b64_e32 v[34:35], v[2:3]
	v_mov_b64_e32 v[62:63], v[14:15]
	v_mov_b64_e32 v[60:61], v[12:13]
	v_mov_b64_e32 v[58:59], v[10:11]
	v_mov_b64_e32 v[56:57], v[8:9]
	v_mov_b64_e32 v[54:55], v[6:7]
	v_mov_b64_e32 v[52:53], v[4:5]
	v_mov_b64_e32 v[50:51], v[2:3]
	v_mov_b32_e32 v244, 0x23ee8
	ds_read2_b64 v[250:253], v244 offset1:1
	ds_read_b64 v[254:255], v244 offset:16
	s_waitcnt lgkmcnt(0)
	v_readfirstlane_b32 s68, v250
	v_readfirstlane_b32 s69, v251
	v_readfirstlane_b32 s70, v252
	v_readfirstlane_b32 s71, v253
	v_readfirstlane_b32 s72, v254
	v_readfirstlane_b32 s73, v255
	ds_read_b64 v[250:251], v244 offset:40
	s_waitcnt lgkmcnt(0)
	v_readfirstlane_b32 s74, v250
	v_readfirstlane_b32 s75, v251
	s_add_u32 s76, s74, 0x16530000
	s_addc_u32 s77, s75, 0
	s_add_u32 s74, s74, 0xa530000
	s_addc_u32 s75, s75, 0
	v_lshrrev_b32_e32 v25, 3, v214
	v_and_b32_e32 v28, 7, v214
	v_lshlrev_b32_e32 v33, 4, v28
	v_lshl_add_u32 v24, v25, 12, v33
	v_lshl_add_u32 v246, v25, 13, v33
	v_mov_b32_e32 v29, 0x120
	v_mul_u32_u24_e32 v29, v29, v28
	v_lshl_add_u32 v29, v25, 1, v29
	s_mul_i32 s2, s40, 2304
	s_cmp_lt_u32 s40, 6
	s_mov_b32 s3, 0x20a00
	s_cselect_b32 s3, 0x20800, s3
	s_add_i32 s2, s2, s3
	v_add_u32_e32 v29, s2, v29
	v_add_u32_e32 v29, 32, v29
	v_mov_b32_e32 v32, 72
	v_mul_u32_u24_e32 v32, v32, v25
	v_lshl_add_u32 v32, v28, 3, v32
	v_add_u32_e32 v32, s2, v32
	s_mul_i32 s66, s96, 8
	s_add_i32 s66, s66, s40
	s_cmpk_lt_u32 s36, 0x100
	s_movk_i32 s67, 112
	s_cselect_b32 s67, 112, s67
	s_cselect_b32 s2, 0, 0x7000
	s_add_i32 s66, s66, s2
	s_add_i32 s90, s67, 6
	s_cmp_eq_u32 s67, 0
	s_cselect_b32 s90, -1, s90
	global_load_dword v249, v24, s[68:69]
	global_load_dword v249, v24, s[68:69]
	s_mov_b32 s32, m0
